# v52 + fma_mix peephole also in k_agg1g2 and k_readout (pairs and single products)
# speedup vs baseline: 1.0216x; 1.0216x over previous
.LBB4_13:
	s_or_b64 exec, exec, s[8:9]
	v_lshlrev_b32_e32 v58, 9, v53
	v_cmp_lt_i32_e32 vcc, v52, v57
	v_or_b32_e32 v1, 0x800, v58
	v_or_b32_e32 v2, v1, v46
	s_waitcnt vmcnt(0)
	v_cndmask_b32_e32 v0, v44, v24, vcc
	ds_write2st64_b32 v2, v0, v50 offset1:1
	v_lshlrev_b32_e32 v50, 2, v55
	v_or_b32_e32 v26, v1, v50
	ds_read2_b32 v[0:1], v26 offset1:4
	ds_read2_b32 v[20:21], v26 offset0:16 offset1:20
	v_lshl_or_b32 v45, v47, 4, v8
	v_cndmask_b32_e32 v59, 0, v25, vcc
	ds_read2_b32 v[24:25], v26 offset0:24 offset1:28
	s_waitcnt lgkmcnt(2)
	v_lshl_add_u32 v0, v0, 7, v45
	s_waitcnt lgkmcnt(1)
	v_lshl_add_u32 v16, v20, 7, v45
	global_load_dwordx4 v[8:11], v0, s[4:5]
	v_lshl_add_u32 v20, v21, 7, v45
	global_load_dwordx4 v[16:19], v16, s[4:5]
	v_lshl_add_u32 v0, v1, 7, v45
	global_load_dwordx4 v[12:15], v0, s[4:5]
	v_or_b32_e32 v27, 0x1000, v58
	global_load_dwordx4 v[20:23], v20, s[4:5]
	ds_read2_b32 v[0:1], v26 offset0:8 offset1:12
	s_waitcnt lgkmcnt(1)
	v_lshl_add_u32 v24, v24, 7, v45
	v_or_b32_e32 v30, v27, v46
	v_or_b32_e32 v60, v27, v50
	s_mov_b32 s3, 48
	s_waitcnt lgkmcnt(0)
	v_lshl_add_u32 v0, v0, 7, v45
	global_load_dwordx4 v[4:7], v0, s[4:5]
	v_lshl_add_u32 v0, v1, 7, v45
	global_load_dwordx4 v[0:3], v0, s[4:5]
	ds_read2_b32 v[28:29], v26 offset0:32 offset1:36
	ds_read2_b32 v[26:27], v26 offset0:40 offset1:44
	global_load_dwordx4 v[40:43], v24, s[4:5]
	ds_write2st64_b32 v30, v59, v51 offset1:1
	v_lshl_add_u32 v24, v25, 7, v45
	s_waitcnt lgkmcnt(2)
	v_lshl_add_u32 v25, v28, 7, v45
	v_lshl_add_u32 v28, v29, 7, v45
	s_waitcnt lgkmcnt(1)
	v_lshl_add_u32 v26, v26, 7, v45
	v_lshl_add_u32 v27, v27, 7, v45
	global_load_dwordx4 v[62:65], v24, s[4:5]
	global_load_dwordx4 v[36:39], v25, s[4:5]
	global_load_dwordx4 v[32:35], v28, s[4:5]
	s_nop 0
	global_load_dwordx4 v[28:31], v26, s[4:5]
	s_nop 0
	global_load_dwordx4 v[24:27], v27, s[4:5]
	v_cmp_lt_i32_e32 vcc, 48, v57
	s_waitcnt vmcnt(11)
	v_cvt_f32_f16_e32 v70, v10
	v_cvt_f32_f16_sdwa v71, v10 dst_sel:DWORD dst_unused:UNUSED_PAD src0_sel:WORD_1
	v_cvt_f32_f16_e32 v66, v8
	v_cvt_f32_f16_sdwa v67, v8 dst_sel:DWORD dst_unused:UNUSED_PAD src0_sel:WORD_1
	s_waitcnt vmcnt(9)
	s_waitcnt vmcnt(8)
	v_cvt_f32_f16_e32 v84, v22
	v_cvt_f32_f16_sdwa v85, v22 dst_sel:DWORD dst_unused:UNUSED_PAD src0_sel:WORD_1
	v_cvt_f32_f16_e32 v91, v23
	v_cvt_f32_f16_e32 v87, v15
	v_cvt_f32_f16_e32 v68, v9
	v_cvt_f32_f16_sdwa v69, v9 dst_sel:DWORD dst_unused:UNUSED_PAD src0_sel:WORD_1
	v_cvt_f32_f16_e32 v72, v12
	v_cvt_f32_f16_sdwa v73, v12 dst_sel:DWORD dst_unused:UNUSED_PAD src0_sel:WORD_1
	s_waitcnt vmcnt(6)
	v_cvt_f32_f16_e32 v78, v1
	v_cvt_f32_f16_sdwa v79, v1 dst_sel:DWORD dst_unused:UNUSED_PAD src0_sel:WORD_1
	v_cvt_f32_f16_sdwa v1, v23 dst_sel:DWORD dst_unused:UNUSED_PAD src0_sel:WORD_1
	ds_read2_b32 v[22:23], v60 offset1:4
	v_cvt_f32_f16_e32 v61, v11
	v_cvt_f32_f16_sdwa v9, v15 dst_sel:DWORD dst_unused:UNUSED_PAD src0_sel:WORD_1
	v_cvt_f32_f16_sdwa v8, v11 dst_sel:DWORD dst_unused:UNUSED_PAD src0_sel:WORD_1
	s_waitcnt lgkmcnt(0)
	v_mov_b32_e32 v86, v23
	v_pk_fma_f32 v[70:71], v[22:23], v[70:71], 0 op_sel_hi:[0,1,0]
	v_fma_mix_f32 v70, v86, v14, v70 op_sel_hi:[0,1,0]
	v_fma_mix_f32 v71, v86, v14, v71 op_sel:[0,1,0] op_sel_hi:[0,1,0]
	ds_read2_b32 v[74:75], v60 offset0:8 offset1:12
	v_cvt_f32_f16_e32 v10, v4
	v_cvt_f32_f16_sdwa v11, v4 dst_sel:DWORD dst_unused:UNUSED_PAD src0_sel:WORD_1
	v_cvt_f32_f16_e32 v14, v5
	v_cvt_f32_f16_sdwa v15, v5 dst_sel:DWORD dst_unused:UNUSED_PAD src0_sel:WORD_1
	v_cvt_f32_f16_e32 v88, v7
	v_cvt_f32_f16_sdwa v4, v7 dst_sel:DWORD dst_unused:UNUSED_PAD src0_sel:WORD_1
	v_pk_fma_f32 v[68:69], v[22:23], v[68:69], 0 op_sel_hi:[0,1,0]
	v_pk_fma_f32 v[66:67], v[22:23], v[66:67], 0 op_sel_hi:[0,1,0]
	v_fma_mix_f32 v12, v86, v13, v68 op_sel_hi:[0,1,0]
	v_fma_mix_f32 v13, v86, v13, v69 op_sel:[0,1,0] op_sel_hi:[0,1,0]
	v_pk_fma_f32 v[66:67], v[86:87], v[72:73], v[66:67] op_sel_hi:[0,1,1]
	s_waitcnt lgkmcnt(0)
	v_pk_fma_f32 v[10:11], v[74:75], v[10:11], v[66:67] op_sel_hi:[0,1,1]
	v_pk_fma_f32 v[12:13], v[74:75], v[14:15], v[12:13] op_sel_hi:[0,1,1]
	v_mov_b32_e32 v14, v75
	v_fma_mix_f32 v66, v74, v6, v70 op_sel_hi:[0,1,0]
	v_fma_mix_f32 v67, v74, v6, v71 op_sel:[0,1,0] op_sel_hi:[0,1,0]
	v_fma_mix_f32 v66, v14, v2, v66 op_sel_hi:[0,1,0]
	v_fma_mix_f32 v67, v14, v2, v67 op_sel:[0,1,0] op_sel_hi:[0,1,0]
	v_pk_fma_f32 v[12:13], v[14:15], v[78:79], v[12:13] op_sel_hi:[0,1,1]
	v_fma_mix_f32 v6, v14, v0, v10 op_sel_hi:[0,1,0]
	v_fma_mix_f32 v7, v14, v0, v11 op_sel:[0,1,0] op_sel_hi:[0,1,0]
	s_waitcnt vmcnt(5)
	v_cvt_f32_f16_e32 v10, v40
	v_cvt_f32_f16_sdwa v11, v40 dst_sel:DWORD dst_unused:UNUSED_PAD src0_sel:WORD_1
	v_cvt_f32_f16_e32 v14, v41
	v_cvt_f32_f16_sdwa v15, v41 dst_sel:DWORD dst_unused:UNUSED_PAD src0_sel:WORD_1
	ds_read2_b32 v[40:41], v60 offset0:16 offset1:20
	v_cvt_f32_f16_e32 v89, v3
	v_cvt_f32_f16_sdwa v5, v3 dst_sel:DWORD dst_unused:UNUSED_PAD src0_sel:WORD_1
	v_cvt_f32_f16_e32 v2, v16
	v_cvt_f32_f16_sdwa v3, v16 dst_sel:DWORD dst_unused:UNUSED_PAD src0_sel:WORD_1
	v_cvt_f32_f16_e32 v16, v17
	v_cvt_f32_f16_sdwa v17, v17 dst_sel:DWORD dst_unused:UNUSED_PAD src0_sel:WORD_1
	v_cvt_f32_f16_e32 v90, v19
	v_cvt_f32_f16_e32 v82, v18
	v_cvt_f32_f16_sdwa v83, v18 dst_sel:DWORD dst_unused:UNUSED_PAD src0_sel:WORD_1
	v_cvt_f32_f16_sdwa v0, v19 dst_sel:DWORD dst_unused:UNUSED_PAD src0_sel:WORD_1
	s_waitcnt lgkmcnt(0)
	v_pk_fma_f32 v[2:3], v[40:41], v[2:3], v[6:7] op_sel_hi:[0,1,1]
	v_pk_fma_f32 v[6:7], v[40:41], v[16:17], v[12:13] op_sel_hi:[0,1,1]
	v_mov_b32_e32 v16, v41
	v_fma_mix_f32 v2, v16, v20, v2 op_sel_hi:[0,1,0]
	v_fma_mix_f32 v3, v16, v20, v3 op_sel:[0,1,0] op_sel_hi:[0,1,0]
	ds_read2_b32 v[18:19], v60 offset0:24 offset1:28
	v_pk_fma_f32 v[12:13], v[40:41], v[82:83], v[66:67] op_sel_hi:[0,1,1]
	v_pk_fma_f32 v[12:13], v[16:17], v[84:85], v[12:13] op_sel_hi:[0,1,1]
	v_fma_mix_f32 v6, v16, v21, v6 op_sel_hi:[0,1,0]
	v_fma_mix_f32 v7, v16, v21, v7 op_sel:[0,1,0] op_sel_hi:[0,1,0]
	s_waitcnt vmcnt(4)
	v_cvt_f32_f16_e32 v20, v62
	v_cvt_f32_f16_sdwa v21, v62 dst_sel:DWORD dst_unused:UNUSED_PAD src0_sel:WORD_1
	v_cvt_f32_f16_e32 v16, v63
	v_cvt_f32_f16_sdwa v17, v63 dst_sel:DWORD dst_unused:UNUSED_PAD src0_sel:WORD_1
	v_pk_mul_f32 v[8:9], v[22:23], v[8:9]
	s_waitcnt lgkmcnt(0)
	v_pk_fma_f32 v[2:3], v[18:19], v[10:11], v[2:3] op_sel_hi:[0,1,1]
	v_fma_mix_f32 v10, v18, v42, v12 op_sel_hi:[0,1,0]
	v_fma_mix_f32 v11, v18, v42, v13 op_sel:[0,1,0] op_sel_hi:[0,1,0]
	v_mov_b32_e32 v12, v19
	s_waitcnt vmcnt(0)
	v_cvt_f32_f16_e32 v66, v26
	v_cvt_f32_f16_sdwa v67, v26 dst_sel:DWORD dst_unused:UNUSED_PAD src0_sel:WORD_1
	v_mul_f32_e32 v22, v22, v61
	v_mul_f32_e32 v26, v23, v87
	v_mov_b32_e32 v23, v8
	v_fma_mix_f32 v10, v12, v64, v10 op_sel_hi:[0,1,0]
	v_fma_mix_f32 v11, v12, v64, v11 op_sel:[0,1,0] op_sel_hi:[0,1,0]
	v_cvt_f32_f16_e32 v62, v30
	v_cvt_f32_f16_sdwa v63, v30 dst_sel:DWORD dst_unused:UNUSED_PAD src0_sel:WORD_1
	v_cvt_f32_f16_e32 v72, v31
	v_cvt_f32_f16_sdwa v30, v31 dst_sel:DWORD dst_unused:UNUSED_PAD src0_sel:WORD_1
	v_cvt_f32_f16_sdwa v31, v27 dst_sel:DWORD dst_unused:UNUSED_PAD src0_sel:WORD_1
	v_cvt_f32_f16_e32 v73, v27
	v_mov_b32_e32 v27, v9
	v_pk_add_f32 v[8:9], v[22:23], 0 op_sel_hi:[1,0]
	v_pk_mul_f32 v[4:5], v[74:75], v[4:5]
	v_pk_add_f32 v[8:9], v[8:9], v[26:27]
	v_mul_f32_e32 v22, v74, v88
	v_mov_b32_e32 v23, v4
	v_pk_add_f32 v[8:9], v[8:9], v[22:23]
	v_mul_f32_e32 v4, v75, v89
	v_pk_mul_f32 v[0:1], v[40:41], v[0:1]
	v_pk_add_f32 v[4:5], v[8:9], v[4:5]
	v_mul_f32_e32 v8, v40, v90
	v_mov_b32_e32 v9, v0
	v_pk_add_f32 v[4:5], v[4:5], v[8:9]
	v_mul_f32_e32 v0, v41, v91
	v_pk_fma_f32 v[6:7], v[18:19], v[14:15], v[6:7] op_sel_hi:[0,1,1]
	v_pk_add_f32 v[0:1], v[4:5], v[0:1]
	ds_read2_b32 v[4:5], v60 offset0:32 offset1:36
	v_pk_fma_f32 v[6:7], v[12:13], v[16:17], v[6:7] op_sel_hi:[0,1,1]
	v_pk_fma_f32 v[2:3], v[12:13], v[20:21], v[2:3] op_sel_hi:[0,1,1]
	v_cvt_f32_f16_e32 v70, v43
	v_cvt_f32_f16_sdwa v42, v43 dst_sel:DWORD dst_unused:UNUSED_PAD src0_sel:WORD_1
	v_cvt_f32_f16_sdwa v43, v65 dst_sel:DWORD dst_unused:UNUSED_PAD src0_sel:WORD_1
	v_cvt_f32_f16_sdwa v20, v39 dst_sel:DWORD dst_unused:UNUSED_PAD src0_sel:WORD_1
	v_cvt_f32_f16_sdwa v21, v35 dst_sel:DWORD dst_unused:UNUSED_PAD src0_sel:WORD_1
	s_waitcnt lgkmcnt(0)
	v_fma_mix_f32 v2, v4, v36, v2 op_sel_hi:[0,1,0]
	v_fma_mix_f32 v3, v4, v36, v3 op_sel:[0,1,0] op_sel_hi:[0,1,0]
	ds_read2_b32 v[12:13], v60 offset0:40 offset1:44
	v_pk_mul_f32 v[8:9], v[18:19], v[42:43]
	v_mul_f32_e32 v22, v18, v70
	v_mov_b32_e32 v23, v8
	v_pk_add_f32 v[0:1], v[0:1], v[22:23]
	v_fma_mix_f32 v8, v19, v65, 0 op_sel_hi:[0,1,0]
	v_pk_mul_f32 v[18:19], v[4:5], v[20:21]
	v_cvt_f32_f16_e32 v64, v24
	v_cvt_f32_f16_sdwa v65, v24 dst_sel:DWORD dst_unused:UNUSED_PAD src0_sel:WORD_1
	v_cvt_f32_f16_e32 v24, v25
	v_cvt_f32_f16_sdwa v25, v25 dst_sel:DWORD dst_unused:UNUSED_PAD src0_sel:WORD_1
	v_fma_mix_f32 v6, v4, v37, v6 op_sel_hi:[0,1,0]
	v_fma_mix_f32 v7, v4, v37, v7 op_sel:[0,1,0] op_sel_hi:[0,1,0]
	v_fma_mix_f32 v14, v4, v39, 0 op_sel_hi:[0,1,0]
	v_pk_add_f32 v[0:1], v[0:1], v[8:9]
	v_mov_b32_e32 v15, v18
	v_fma_mix_f32 v10, v4, v38, v10 op_sel_hi:[0,1,0]
	v_fma_mix_f32 v11, v4, v38, v11 op_sel:[0,1,0] op_sel_hi:[0,1,0]
	v_fma_mix_f32 v16, v5, v35, 0 op_sel_hi:[0,1,0]
	v_mov_b32_e32 v20, v5
	s_waitcnt lgkmcnt(0)
	v_pk_mul_f32 v[26:27], v[12:13], v[30:31]
	v_pk_add_f32 v[0:1], v[0:1], v[14:15]
	v_mov_b32_e32 v17, v19
	v_mul_f32_e32 v4, v12, v72
	v_fma_mix_f32 v10, v20, v34, v10 op_sel_hi:[0,1,0]
	v_fma_mix_f32 v11, v20, v34, v11 op_sel:[0,1,0] op_sel_hi:[0,1,0]
	v_fma_mix_f32 v6, v20, v33, v6 op_sel_hi:[0,1,0]
	v_fma_mix_f32 v7, v20, v33, v7 op_sel:[0,1,0] op_sel_hi:[0,1,0]
	v_fma_mix_f32 v2, v20, v32, v2 op_sel_hi:[0,1,0]
	v_fma_mix_f32 v3, v20, v32, v3 op_sel:[0,1,0] op_sel_hi:[0,1,0]
	v_pk_add_f32 v[0:1], v[0:1], v[16:17]
	v_mov_b32_e32 v5, v26
	v_mov_b32_e32 v22, v13
	v_mul_f32_e32 v8, v13, v73
	v_pk_add_f32 v[14:15], v[0:1], v[4:5]
	v_fma_mix_f32 v0, v12, v28, v2 op_sel_hi:[0,1,0]
	v_fma_mix_f32 v1, v12, v28, v3 op_sel:[0,1,0] op_sel_hi:[0,1,0]
	v_fma_mix_f32 v2, v12, v29, v6 op_sel_hi:[0,1,0]
	v_fma_mix_f32 v3, v12, v29, v7 op_sel:[0,1,0] op_sel_hi:[0,1,0]
	v_pk_fma_f32 v[4:5], v[12:13], v[62:63], v[10:11] op_sel_hi:[0,1,1]
	v_mov_b32_e32 v9, v27
	v_pk_fma_f32 v[4:5], v[22:23], v[66:67], v[4:5] op_sel_hi:[0,1,1]
	v_pk_fma_f32 v[2:3], v[22:23], v[24:25], v[2:3] op_sel_hi:[0,1,1]
	v_pk_fma_f32 v[0:1], v[22:23], v[64:65], v[0:1] op_sel_hi:[0,1,1]
	v_pk_add_f32 v[6:7], v[14:15], v[8:9]
	s_and_saveexec_b64 s[8:9], vcc
	s_cbranch_execz .LBB4_17
	s_movk_i32 s10, 0x8c0
	v_or3_b32 v24, v58, v50, s10
	s_mov_b64 s[10:11], 0
